# differential-attention tile-skip test: the five key-norm loads issued together (one memory round trip instead of three)
# speedup vs baseline: 1.0046x; 1.0046x over previous
; __device__ __forceinline__ float knt(const float* kn2, int t) { const f32x4 p = *(const f32x4*)(kn2 + 4 * t); return sqrtf((p[0] + p[1]) + (p[2] + p[3])) * 1.005f; }
; template <bool MOBA>
; __device__ __forceinline__ void run_unit(const UnitDesc& U, LAS unsigned char* lds, f32x16 (&o)[4], float (&rli)[16]) {
;     ...
;             float qm = wm[0];
; #pragma unroll
;             for (int w = 1; w < 8; ++w) qm = fmaxf(qm, wm[w]);
;             const float qc = sqrtf(qm) * (CS * 1.0005f); const int NTd = U.nt - 4;
;             const float kown = fmaxf(fmaxf(knt(U.knorm, NTd), knt(U.knorm, NTd + 1)), fmaxf(knt(U.knorm, NTd + 2), knt(U.knorm, NTd + 3)));
;             bool ns = false;
;             if (lane < NTd) ns = !(U.slopeL * (float)(U.q0 - KVBLK * lane - (KVBLK - 1)) > fmaf(qc, knt(U.knorm, lane) + kown, 35.0f));
;             const unsigned long long mk = __ballot(ns);
;             if (lane == 0) *tmin = (mk ? (int)__builtin_ctzll(mk) : NTd) & ~1;
.LBB0_805:
	s_or_b64 exec, exec, s[0:1]
	s_cmp_gt_u32 s67, 63
	s_waitcnt lgkmcnt(0)
	s_barrier
	s_cbranch_scc1 .LBB0_811
	v_readlane_b32 s0, v254, 57
	s_mov_b64 s[6:7], 0
	s_nop 0
	v_cmp_gt_i32_e64 s[0:1], s0, v186
	s_and_saveexec_b64 s[8:9], s[0:1]
	s_cbranch_execz .LBB0_808
	v_readlane_b32 s0, v254, 56
	s_or_b32 s0, s12, s0
	s_ashr_i32 s1, s0, 31
	s_lshl_b64 s[0:1], s[0:1], 2
	v_readlane_b32 s6, v254, 30
	s_add_u32 s10, s6, s0
	v_readlane_b32 s0, v254, 31
	s_addc_u32 s11, s0, s1
	v_readlane_b32 s0, v255, 0
	v_readlane_b32 s1, v255, 1
	s_add_u32 s0, s10, s0
	s_addc_u32 s1, s11, s1
	v_lshlrev_b32_e32 v34, 4, v186
	global_load_dwordx4 v[38:41], v3, s[0:1]
	v_readlane_b32 s0, v255, 2
	v_readlane_b32 s1, v255, 3
	s_add_u32 s0, s10, s0
	s_addc_u32 s1, s11, s1
	global_load_dwordx4 v[22:25], v3, s[0:1] offset:-16
	global_load_dwordx4 v[26:29], v3, s[0:1] offset:-32
	global_load_dwordx4 v[14:17], v3, s[0:1] offset:-48
	global_load_dwordx4 v[30:33], v34, s[10:11]
	v_readlane_b32 s0, v253, 28
	s_mov_b32 s13, 0xf800000
	s_nop 0
	v_mov_b32_e32 v4, s0
	ds_read_b128 v[4:7], v4
	v_readlane_b32 s0, v253, 29
	s_waitcnt lgkmcnt(0)
	v_max_f32_e32 v5, v5, v5
	v_max_f32_e32 v4, v4, v4
	v_max_f32_e32 v4, v4, v5
	v_max3_f32 v9, v4, v6, v7
	v_mov_b32_e32 v4, s0
	ds_read_b128 v[4:7], v4
	s_waitcnt lgkmcnt(0)
	v_max3_f32 v4, v9, v4, v5
	v_max3_f32 v20, v4, v6, v7
	s_waitcnt vmcnt(4)
	v_mov_b32_e32 v4, v38
	v_mov_b32_e32 v5, v39
	v_mov_b32_e32 v6, v40
	v_mov_b32_e32 v7, v41
	v_mov_b32_e32 v10, v5
	v_mov_b32_e32 v11, v6
	v_mov_b32_e32 v5, v7
	v_pk_add_f32 v[4:5], v[10:11], v[4:5]
	s_nop 0
	v_add_f32_e32 v4, v4, v5
	v_cmp_gt_f32_e64 s[0:1], s13, v4
	v_mul_f32_e32 v5, 0x4f800000, v4
	s_nop 0
	v_cndmask_b32_e64 v4, v4, v5, s[0:1]
	v_sqrt_f32_e32 v5, v4
	s_nop 0
	v_add_u32_e32 v6, -1, v5
	v_fma_f32 v7, -v6, v5, v4
	v_cmp_ge_f32_e64 s[6:7], 0, v7
	v_add_u32_e32 v7, 1, v5
	s_nop 0
	v_cndmask_b32_e64 v6, v5, v6, s[6:7]
	v_fma_f32 v5, -v7, v5, v4
	v_cmp_lt_f32_e64 s[6:7], 0, v5
	s_nop 1
	v_cndmask_b32_e64 v5, v6, v7, s[6:7]
	v_mul_f32_e32 v6, 0x37800000, v5
	v_cndmask_b32_e64 v5, v5, v6, s[0:1]
	v_cmp_class_f32_e64 s[0:1], v4, v225
	s_nop 1
	v_cndmask_b32_e64 v4, v5, v4, s[0:1]
	v_mul_f32_e32 v9, 0x3f80a3d7, v4
	s_waitcnt vmcnt(1)
	v_mov_b32_e32 v4, v22
	v_mov_b32_e32 v5, v23
	v_mov_b32_e32 v6, v24
	v_mov_b32_e32 v7, v25
	v_mov_b32_e32 v10, v26
	v_mov_b32_e32 v11, v27
	v_mov_b32_e32 v12, v28
	v_mov_b32_e32 v13, v29
	v_mov_b32_e32 v18, v15
	v_mov_b32_e32 v19, v16
	v_mov_b32_e32 v15, v17
	v_pk_add_f32 v[14:15], v[18:19], v[14:15]
	s_nop 0
	v_add_f32_e32 v14, v14, v15
	v_cmp_gt_f32_e64 s[0:1], s13, v14
	v_mul_f32_e32 v15, 0x4f800000, v14
	s_nop 0
	v_cndmask_b32_e64 v14, v14, v15, s[0:1]
	v_sqrt_f32_e32 v15, v14
	s_nop 0
	v_add_u32_e32 v16, -1, v15
	v_fma_f32 v17, -v16, v15, v14
	v_cmp_ge_f32_e64 s[6:7], 0, v17
	v_add_u32_e32 v17, 1, v15
	s_nop 0
	v_cndmask_b32_e64 v16, v15, v16, s[6:7]
	v_fma_f32 v15, -v17, v15, v14
	v_cmp_lt_f32_e64 s[6:7], 0, v15
	s_nop 1
	v_cndmask_b32_e64 v15, v16, v17, s[6:7]
	v_mul_f32_e32 v16, 0x37800000, v15
	v_cndmask_b32_e64 v15, v15, v16, s[0:1]
	v_cmp_class_f32_e64 s[0:1], v14, v225
	s_nop 1
	v_cndmask_b32_e64 v14, v15, v14, s[0:1]
	v_mul_f32_e32 v16, 0x3f80a3d7, v14
	v_mov_b32_e32 v14, v11
	v_mov_b32_e32 v15, v12
	v_mov_b32_e32 v11, v13
	v_pk_add_f32 v[10:11], v[14:15], v[10:11]
	s_nop 0
	v_add_f32_e32 v10, v10, v11
	v_cmp_gt_f32_e64 s[0:1], s13, v10
	v_mul_f32_e32 v11, 0x4f800000, v10
	s_nop 0
	v_cndmask_b32_e64 v10, v10, v11, s[0:1]
	v_sqrt_f32_e32 v11, v10
	s_nop 0
	v_add_u32_e32 v12, -1, v11
	v_fma_f32 v13, -v12, v11, v10
	v_cmp_ge_f32_e64 s[6:7], 0, v13
	v_add_u32_e32 v13, 1, v11
	s_nop 0
	v_cndmask_b32_e64 v12, v11, v12, s[6:7]
	v_fma_f32 v11, -v13, v11, v10
	v_cmp_lt_f32_e64 s[6:7], 0, v11
	s_nop 1
	v_cndmask_b32_e64 v11, v12, v13, s[6:7]
	v_mul_f32_e32 v12, 0x37800000, v11
	v_cndmask_b32_e64 v11, v11, v12, s[0:1]
	v_cmp_class_f32_e64 s[0:1], v10, v225
	s_nop 1
	v_cndmask_b32_e64 v10, v11, v10, s[0:1]
	v_mul_f32_e32 v12, 0x3f80a3d7, v10
	v_mov_b32_e32 v10, v5
	v_mov_b32_e32 v11, v6
	v_mov_b32_e32 v5, v7
	v_pk_add_f32 v[4:5], v[10:11], v[4:5]
	s_nop 0
	v_add_f32_e32 v4, v4, v5
	v_cmp_gt_f32_e64 s[0:1], s13, v4
	v_mul_f32_e32 v5, 0x4f800000, v4
	s_nop 0
	v_cndmask_b32_e64 v4, v4, v5, s[0:1]
	v_sqrt_f32_e32 v5, v4
	s_nop 0
	v_add_u32_e32 v6, -1, v5
	v_fma_f32 v7, -v6, v5, v4
	v_cmp_ge_f32_e64 s[6:7], 0, v7
	v_add_u32_e32 v7, 1, v5
	s_nop 0
	v_cndmask_b32_e64 v6, v5, v6, s[6:7]
	v_fma_f32 v5, -v7, v5, v4
	v_cmp_lt_f32_e64 s[6:7], 0, v5
	s_nop 1
	v_cndmask_b32_e64 v5, v6, v7, s[6:7]
	v_mul_f32_e32 v6, 0x37800000, v5
	v_cndmask_b32_e64 v5, v5, v6, s[0:1]
	v_cmp_class_f32_e64 s[0:1], v4, v225
	s_nop 1
	v_cndmask_b32_e64 v4, v5, v4, s[0:1]
	v_mul_f32_e32 v4, 0x3f80a3d7, v4
	v_max_f32_e32 v4, v12, v4
	v_max3_f32 v9, v9, v16, v4
	v_cmp_gt_f32_e64 s[0:1], s13, v20
	v_mul_f32_e32 v4, 0x4f800000, v20
	s_nop 0
	v_cndmask_b32_e64 v4, v20, v4, s[0:1]
	v_sqrt_f32_e32 v5, v4
	s_nop 0
	v_add_u32_e32 v6, -1, v5
	v_fma_f32 v7, -v6, v5, v4
	v_cmp_ge_f32_e64 s[6:7], 0, v7
	v_add_u32_e32 v7, 1, v5
	s_nop 0
	v_cndmask_b32_e64 v6, v5, v6, s[6:7]
	v_fma_f32 v5, -v7, v5, v4
	v_cmp_lt_f32_e64 s[6:7], 0, v5
	s_nop 1
	v_cndmask_b32_e64 v5, v6, v7, s[6:7]
	v_mul_f32_e32 v6, 0x37800000, v5
	v_cndmask_b32_e64 v5, v5, v6, s[0:1]
	v_cmp_class_f32_e64 s[0:1], v4, v225
	s_nop 1
	v_cndmask_b32_e64 v4, v5, v4, s[0:1]
	v_mul_f32_e32 v10, 0x3e02a4a4, v4
	v_lshlrev_b32_e32 v4, 6, v186
	v_readlane_b32 s0, v254, 60
	s_nop 1
	v_sub_u32_e32 v4, s0, v4
	v_cvt_f32_i32_e32 v4, v4
	v_mul_f32_e32 v11, v196, v4
	s_waitcnt vmcnt(0)
	v_mov_b32_e32 v4, v30
	v_mov_b32_e32 v5, v31
	v_mov_b32_e32 v6, v32
	v_mov_b32_e32 v7, v33
	v_mov_b32_e32 v12, v5
	v_mov_b32_e32 v13, v6
	v_mov_b32_e32 v5, v7
	v_pk_add_f32 v[4:5], v[12:13], v[4:5]
	s_nop 0
	v_add_f32_e32 v4, v4, v5
	v_cmp_gt_f32_e64 s[0:1], s13, v4
	v_mul_f32_e32 v5, 0x4f800000, v4
	s_nop 0
	v_cndmask_b32_e64 v4, v4, v5, s[0:1]
	v_sqrt_f32_e32 v5, v4
	s_nop 0
	v_add_u32_e32 v6, -1, v5
	v_fma_f32 v7, -v6, v5, v4
	v_cmp_ge_f32_e64 s[6:7], 0, v7
	v_add_u32_e32 v7, 1, v5
	s_nop 0
	v_cndmask_b32_e64 v6, v5, v6, s[6:7]
	v_fma_f32 v5, -v7, v5, v4
	v_cmp_lt_f32_e64 s[6:7], 0, v5
	s_nop 1
	v_cndmask_b32_e64 v5, v6, v7, s[6:7]
	v_mul_f32_e32 v6, 0x37800000, v5
	v_cndmask_b32_e64 v5, v5, v6, s[0:1]
	v_cmp_class_f32_e64 s[0:1], v4, v225
	s_nop 1
	v_cndmask_b32_e64 v4, v5, v4, s[0:1]
	v_fmac_f32_e32 v9, 0x3f80a3d7, v4
	v_fmaak_f32 v4, v10, v9, 0x420c0000
	v_cmp_ngt_f32_e64 s[0:1], v11, v4
	s_and_b64 s[6:7], s[0:1], exec
